# stack + up-proj epilogue row-scale partial loads requested in two batches (row groups 1-3 behind group 0, 5-7 behind group 4) with counted vmcnt
# baseline (speedup 1.0000x reference)
.LBB0_400:
	s_lshl_b32 s48, s8, 8
	s_cmp_lg_u32 s58, 0
	v_mbcnt_lo_u32_b32 v112, -1, 0
	v_mbcnt_hi_u32_b32 v112, -1, v112
	s_cselect_b64 s[62:63], -1, 0
	v_and_b32_e32 v237, 15, v112
	s_cmp_eq_u32 s58, 0
	v_or_b32_e32 v231, s85, v237
	s_cselect_b32 s6, 0, 32
	v_add_u32_e32 v232, s48, v231
	s_add_u32 s16, s77, s6
	v_ashrrev_i32_e32 v233, 31, v232
	s_addc_u32 s17, s78, 0
	v_lshlrev_b64 v[114:115], 6, v[232:233]
	v_lshl_add_u64 v[118:119], s[16:17], 0, v[114:115]
	global_load_dwordx4 v[114:117], v[118:119], off
	global_load_dwordx4 v[128:131], v[118:119], off offset:16
	global_load_dwordx4 v[140:143], v[118:119], off offset:1024
	global_load_dwordx4 v[144:147], v[118:119], off offset:1040
	global_load_dwordx4 v[148:151], v[118:119], off offset:2048
	global_load_dwordx4 v[192:195], v[118:119], off offset:2064
	global_load_dwordx4 v[242:245], v[118:119], off offset:3072
	global_load_dwordx4 v[246:249], v[118:119], off offset:3088
	v_mul_f32_e32 v118, v157, v157
	v_mul_f32_e32 v119, v159, v159
	v_mul_f32_e32 v132, v153, v153
	v_mul_f32_e32 v133, v155, v155
	v_fmac_f32_e32 v118, v156, v156
	v_fmac_f32_e32 v119, v158, v158
	v_fmac_f32_e32 v132, v152, v152
	v_fmac_f32_e32 v133, v154, v154
	v_add_f32_e32 v118, v118, v119
	v_ashrrev_i32_e32 v135, 2, v112
	v_cndmask_b32_e64 v134, 0, 1, s[44:45]
	v_and_b32_e32 v208, -4, v135
	s_mov_b64 s[10:11], -1
	v_cmp_ne_u32_e64 s[6:7], 1, v134
	v_ashrrev_i32_e32 v209, 31, v208
	s_waitcnt vmcnt(7)
	v_add_f32_e32 v114, v114, v115
	v_add_f32_e32 v115, v116, v117
	s_waitcnt vmcnt(6)
	v_add_f32_e32 v116, v128, v129
	v_add_f32_e32 v117, v130, v131
	v_add_f32_e32 v114, v114, v115
	v_add_f32_e32 v115, v116, v117
	v_add_f32_e32 v114, v114, v115
	v_fmamk_f32 v114, v114, 0x3b000000, v213
	v_mul_f32_e32 v115, 0x4f800000, v114
	v_cmp_gt_f32_e32 vcc, s90, v114
	s_nop 1
	v_cndmask_b32_e32 v115, v114, v115, vcc
	v_sqrt_f32_e32 v116, v115
	v_add_f32_e32 v114, v132, v133
	v_add_f32_e32 v114, v118, v114
	v_add_u32_e32 v117, -1, v116
	v_add_u32_e32 v118, 1, v116
	v_fma_f32 v119, -v117, v116, v115
	v_fma_f32 v128, -v118, v116, v115
	v_cmp_ge_f32_e64 s[8:9], 0, v119
	s_nop 1
	v_cndmask_b32_e64 v116, v116, v117, s[8:9]
	v_cmp_lt_f32_e64 s[8:9], 0, v128
	s_nop 1
	v_cndmask_b32_e64 v116, v116, v118, s[8:9]
	v_mul_f32_e32 v117, 0x37800000, v116
	v_cndmask_b32_e32 v116, v116, v117, vcc
	v_cmp_class_f32_e32 vcc, v115, v215
	s_nop 1
	v_cndmask_b32_e32 v115, v116, v115, vcc
	v_div_scale_f32 v116, s[8:9], v115, v115, 1.0
	v_rcp_f32_e32 v117, v116
	v_div_scale_f32 v118, vcc, 1.0, v115, 1.0
	s_and_b64 s[8:9], exec, s[62:63]
	v_fma_f32 v119, -v116, v117, 1.0
	v_fmac_f32_e32 v117, v119, v117
	v_mul_f32_e32 v119, v118, v117
	v_fma_f32 v128, -v116, v119, v118
	v_fmac_f32_e32 v119, v128, v117
	v_fma_f32 v116, -v116, v119, v118
	v_div_fmas_f32 v116, v116, v117, v119
	v_div_fixup_f32 v236, v116, v115, 1.0
	v_mul_f32_e32 v115, v236, v236
	s_mov_b64 vcc, s[8:9]
	s_cbranch_vccz .LBB0_404
	s_and_b64 vcc, exec, s[6:7]
	v_mul_f32_e32 v113, v114, v115
	s_cbranch_vccnz .LBB0_403
	v_mov_b64_e32 v[116:117], s[50:51]
	v_mad_i64_i32 v[116:117], s[8:9], v232, s65, v[116:117]
	v_lshl_add_u64 v[116:117], v[208:209], 1, v[116:117]
	global_load_dwordx2 v[160:161], v[116:117], off offset:2080
	global_load_dwordx2 v[162:163], v[116:117], off offset:2048
	v_add_u32_e32 v118, 0x10, v232
	v_mov_b64_e32 v[116:117], s[50:51]
	v_mad_i64_i32 v[116:117], s[8:9], v118, s65, v[116:117]
	v_lshl_add_u64 v[116:117], v[208:209], 1, v[116:117]
	global_load_dwordx2 v[164:165], v[116:117], off offset:2080
	global_load_dwordx2 v[166:167], v[116:117], off offset:2048
	v_add_u32_e32 v118, 0x20, v232
	v_mov_b64_e32 v[116:117], s[50:51]
	v_mad_i64_i32 v[116:117], s[8:9], v118, s65, v[116:117]
	v_lshl_add_u64 v[116:117], v[208:209], 1, v[116:117]
	global_load_dwordx2 v[168:169], v[116:117], off offset:2080
	global_load_dwordx2 v[170:171], v[116:117], off offset:2048
	v_add_u32_e32 v118, 0x30, v232
	v_mov_b64_e32 v[116:117], s[50:51]
	v_mad_i64_i32 v[116:117], s[8:9], v118, s65, v[116:117]
	v_lshl_add_u64 v[116:117], v[208:209], 1, v[116:117]
	global_load_dwordx2 v[172:173], v[116:117], off offset:2080
	global_load_dwordx2 v[174:175], v[116:117], off offset:2048
	v_add_u32_e32 v118, 0x80, v232
	v_mov_b64_e32 v[116:117], s[50:51]
	v_mad_i64_i32 v[116:117], s[8:9], v118, s65, v[116:117]
	v_lshl_add_u64 v[116:117], v[208:209], 1, v[116:117]
	global_load_dwordx2 v[176:177], v[116:117], off offset:2080
	global_load_dwordx2 v[178:179], v[116:117], off offset:2048
	v_add_u32_e32 v118, 0x90, v232
	v_mov_b64_e32 v[116:117], s[50:51]
	v_mad_i64_i32 v[116:117], s[8:9], v118, s65, v[116:117]
	v_lshl_add_u64 v[116:117], v[208:209], 1, v[116:117]
	global_load_dwordx2 v[180:181], v[116:117], off offset:2080
	global_load_dwordx2 v[182:183], v[116:117], off offset:2048
	v_add_u32_e32 v118, 0xa0, v232
	v_mov_b64_e32 v[116:117], s[50:51]
	v_mad_i64_i32 v[116:117], s[8:9], v118, s65, v[116:117]
	v_lshl_add_u64 v[116:117], v[208:209], 1, v[116:117]
	global_load_dwordx2 v[184:185], v[116:117], off offset:2080
	global_load_dwordx2 v[186:187], v[116:117], off offset:2048
	v_add_u32_e32 v118, 0xb0, v232
	v_mov_b64_e32 v[116:117], s[50:51]
	v_mad_i64_i32 v[116:117], s[8:9], v118, s65, v[116:117]
	v_lshl_add_u64 v[116:117], v[208:209], 1, v[116:117]
	global_load_dwordx2 v[188:189], v[116:117], off offset:2080
	global_load_dwordx2 v[190:191], v[116:117], off offset:2048
	s_waitcnt vmcnt(14)
	v_lshlrev_b32_e32 v129, 16, v160
	v_and_b32_e32 v131, 0xffff0000, v160
	v_and_b32_e32 v130, 0xffff0000, v162
	v_lshlrev_b32_e32 v133, 16, v161
	v_and_b32_e32 v119, 0xffff0000, v161
	v_and_b32_e32 v118, 0xffff0000, v163
	v_lshlrev_b32_e32 v128, 16, v162
	v_lshlrev_b32_e32 v132, 16, v163
	v_pk_mul_f32 v[116:117], v[130:131], v[130:131]
	v_pk_mul_f32 v[118:119], v[118:119], v[118:119]
	v_pk_fma_f32 v[116:117], v[128:129], v[128:129], v[116:117]
	v_pk_fma_f32 v[118:119], v[132:133], v[132:133], v[118:119]
	s_nop 0
	v_pk_add_f32 v[116:117], v[116:117], v[118:119]
	s_nop 0
	v_add_f32_e32 v113, v113, v116
	v_add_f32_e32 v113, v113, v117

.LBB0_410:
	s_or_b64 exec, exec, s[8:9]
	v_or_b32_e32 v238, 16, v232
	v_ashrrev_i32_e32 v239, 31, v238
	v_lshlrev_b64 v[112:113], 6, v[238:239]
	v_lshl_add_u64 v[112:113], s[16:17], 0, v[112:113]
	v_mul_f32_e32 v112, v109, v109
	v_mul_f32_e32 v113, v111, v111
	s_waitcnt lgkmcnt(0)
	v_mul_f32_e32 v117, v105, v105
	v_mul_f32_e32 v118, v107, v107
	v_fmac_f32_e32 v112, v108, v108
	v_fmac_f32_e32 v113, v110, v110
	v_fmac_f32_e32 v117, v104, v104
	v_fmac_f32_e32 v118, v106, v106
	v_cndmask_b32_e64 v119, 0, 1, s[62:63]
	v_add_f32_e32 v112, v112, v113
	v_add_f32_e32 v113, v117, v118
	v_cmp_ne_u32_e64 s[8:9], 1, v119
	v_add_f32_e32 v112, v112, v113
	s_mov_b64 s[26:27], -1
	s_waitcnt vmcnt(5)
	v_add_f32_e32 v128, v140, v141
	v_add_f32_e32 v129, v142, v143
	s_waitcnt vmcnt(4)
	v_add_f32_e32 v130, v144, v145
	v_add_f32_e32 v131, v146, v147
	v_add_f32_e32 v128, v128, v129
	v_add_f32_e32 v129, v130, v131
	v_add_f32_e32 v128, v128, v129
	v_fmamk_f32 v128, v128, 0x3b000000, v213
	v_mul_f32_e32 v129, 0x4f800000, v128
	v_cmp_gt_f32_e32 vcc, s90, v128
	s_nop 1
	v_cndmask_b32_e32 v128, v128, v129, vcc
	v_sqrt_f32_e32 v129, v128
	s_nop 0
	v_add_u32_e32 v117, -1, v129
	v_add_u32_e32 v118, 1, v129
	v_fma_f32 v119, -v117, v129, v128
	v_fma_f32 v130, -v118, v129, v128
	v_cmp_ge_f32_e64 s[14:15], 0, v119
	s_nop 1
	v_cndmask_b32_e64 v117, v129, v117, s[14:15]
	v_cmp_lt_f32_e64 s[14:15], 0, v130
	s_nop 1
	v_cndmask_b32_e64 v117, v117, v118, s[14:15]
	v_mul_f32_e32 v118, 0x37800000, v117
	v_cndmask_b32_e32 v117, v117, v118, vcc
	v_cmp_class_f32_e32 vcc, v128, v215
	s_nop 1
	v_cndmask_b32_e32 v117, v117, v128, vcc
	v_div_scale_f32 v118, s[14:15], v117, v117, 1.0
	v_rcp_f32_e32 v119, v118
	v_div_scale_f32 v113, vcc, 1.0, v117, 1.0
	v_fma_f32 v128, -v118, v119, 1.0
	v_fmac_f32_e32 v119, v128, v119
	v_mul_f32_e32 v128, v113, v119
	v_fma_f32 v129, -v118, v128, v113
	v_fmac_f32_e32 v128, v129, v119
	v_fma_f32 v113, -v118, v128, v113
	v_div_fmas_f32 v113, v113, v119, v128
	v_div_fixup_f32 v132, v113, v117, 1.0
	s_andn2_b64 vcc, exec, s[62:63]
	v_mul_f32_e32 v113, v132, v132
	s_cbranch_vccnz .LBB0_414
	s_and_b64 vcc, exec, s[6:7]
	v_mul_f32_e32 v117, v112, v113
	s_cbranch_vccnz .LBB0_413
	v_lshlrev_b32_e32 v131, 16, v164
	v_and_b32_e32 v135, 0xffff0000, v164
	v_and_b32_e32 v134, 0xffff0000, v166
	v_lshlrev_b32_e32 v137, 16, v165
	v_and_b32_e32 v129, 0xffff0000, v165
	v_and_b32_e32 v128, 0xffff0000, v167
	v_lshlrev_b32_e32 v130, 16, v166
	v_lshlrev_b32_e32 v136, 16, v167
	v_pk_mul_f32 v[118:119], v[134:135], v[134:135]
	v_pk_mul_f32 v[128:129], v[128:129], v[128:129]
	v_pk_fma_f32 v[118:119], v[130:131], v[130:131], v[118:119]
	v_pk_fma_f32 v[128:129], v[136:137], v[136:137], v[128:129]
	s_nop 0
	v_pk_add_f32 v[118:119], v[118:119], v[128:129]
	s_nop 0
	v_add_f32_e32 v117, v117, v118
	v_add_f32_e32 v117, v117, v119

.LBB0_420:
	s_or_b64 exec, exec, s[14:15]
	v_or_b32_e32 v228, 32, v232
	v_ashrrev_i32_e32 v229, 31, v228
	s_waitcnt lgkmcnt(0)
	v_lshlrev_b64 v[112:113], 6, v[228:229]
	v_lshl_add_u64 v[112:113], s[16:17], 0, v[112:113]
	v_mul_f32_e32 v112, v93, v93
	v_mul_f32_e32 v113, v95, v95
	v_mul_f32_e32 v117, v89, v89
	v_mul_f32_e32 v118, v91, v91
	v_fmac_f32_e32 v112, v92, v92
	v_fmac_f32_e32 v113, v94, v94
	v_fmac_f32_e32 v117, v88, v88
	v_fmac_f32_e32 v118, v90, v90
	v_add_f32_e32 v112, v112, v113
	v_add_f32_e32 v113, v117, v118
	v_add_f32_e32 v112, v112, v113
	s_mov_b64 s[26:27], -1
	s_waitcnt vmcnt(3)
	v_add_f32_e32 v119, v148, v149
	v_add_f32_e32 v128, v150, v151
	s_waitcnt vmcnt(2)
	v_add_f32_e32 v129, v192, v193
	v_add_f32_e32 v130, v194, v195
	v_add_f32_e32 v119, v119, v128
	v_add_f32_e32 v128, v129, v130
	v_add_f32_e32 v119, v119, v128
	v_fmamk_f32 v119, v119, 0x3b000000, v213
	v_mul_f32_e32 v128, 0x4f800000, v119
	v_cmp_gt_f32_e32 vcc, s90, v119
	s_nop 1
	v_cndmask_b32_e32 v119, v119, v128, vcc
	v_sqrt_f32_e32 v128, v119
	s_nop 0
	v_add_u32_e32 v117, -1, v128
	v_add_u32_e32 v118, 1, v128
	v_fma_f32 v129, -v117, v128, v119
	v_fma_f32 v130, -v118, v128, v119
	v_cmp_ge_f32_e64 s[14:15], 0, v129
	s_nop 1
	v_cndmask_b32_e64 v117, v128, v117, s[14:15]
	v_cmp_lt_f32_e64 s[14:15], 0, v130
	s_nop 1
	v_cndmask_b32_e64 v117, v117, v118, s[14:15]
	v_mul_f32_e32 v118, 0x37800000, v117
	v_cndmask_b32_e32 v117, v117, v118, vcc
	v_cmp_class_f32_e32 vcc, v119, v215
	s_nop 1
	v_cndmask_b32_e32 v117, v117, v119, vcc
	v_div_scale_f32 v118, s[14:15], v117, v117, 1.0
	v_rcp_f32_e32 v119, v118
	v_div_scale_f32 v113, vcc, 1.0, v117, 1.0
	v_fma_f32 v128, -v118, v119, 1.0
	v_fmac_f32_e32 v119, v128, v119
	v_mul_f32_e32 v128, v113, v119
	v_fma_f32 v129, -v118, v128, v113
	v_fmac_f32_e32 v128, v129, v119
	v_fma_f32 v113, -v118, v128, v113
	v_div_fmas_f32 v113, v113, v119, v128
	v_div_fixup_f32 v230, v113, v117, 1.0
	s_and_b64 vcc, exec, s[8:9]
	v_mul_f32_e32 v113, v230, v230
	s_cbranch_vccnz .LBB0_424
	s_and_b64 vcc, exec, s[6:7]
	v_mul_f32_e32 v117, v112, v113
	s_cbranch_vccnz .LBB0_423
	v_lshlrev_b32_e32 v131, 16, v168
	v_and_b32_e32 v135, 0xffff0000, v168
	v_and_b32_e32 v134, 0xffff0000, v170
	v_lshlrev_b32_e32 v137, 16, v169
	v_and_b32_e32 v129, 0xffff0000, v169
	v_and_b32_e32 v128, 0xffff0000, v171
	v_lshlrev_b32_e32 v130, 16, v170
	v_lshlrev_b32_e32 v136, 16, v171
	v_pk_mul_f32 v[118:119], v[134:135], v[134:135]
	v_pk_mul_f32 v[128:129], v[128:129], v[128:129]
	v_pk_fma_f32 v[118:119], v[130:131], v[130:131], v[118:119]
	v_pk_fma_f32 v[128:129], v[136:137], v[136:137], v[128:129]
	s_nop 0
	v_pk_add_f32 v[118:119], v[118:119], v[128:129]
	s_nop 0
	v_add_f32_e32 v117, v117, v118
	v_add_f32_e32 v117, v117, v119

.LBB0_430:
	s_or_b64 exec, exec, s[14:15]
	v_or_b32_e32 v234, 48, v232
	v_ashrrev_i32_e32 v235, 31, v234
	s_waitcnt lgkmcnt(0)
	v_lshlrev_b64 v[112:113], 6, v[234:235]
	v_lshl_add_u64 v[112:113], s[16:17], 0, v[112:113]
	v_mul_f32_e32 v112, v77, v77
	v_mul_f32_e32 v113, v79, v79
	v_mul_f32_e32 v117, v73, v73
	v_mul_f32_e32 v118, v75, v75
	v_fmac_f32_e32 v112, v76, v76
	v_fmac_f32_e32 v113, v78, v78
	v_fmac_f32_e32 v117, v72, v72
	v_fmac_f32_e32 v118, v74, v74
	v_add_f32_e32 v112, v112, v113
	v_add_f32_e32 v113, v117, v118
	v_add_f32_e32 v112, v112, v113
	s_mov_b64 s[26:27], -1
	s_waitcnt vmcnt(1)
	v_add_f32_e32 v119, v242, v243
	v_add_f32_e32 v128, v244, v245
	s_waitcnt vmcnt(0)
	v_add_f32_e32 v129, v246, v247
	v_add_f32_e32 v130, v248, v249
	v_add_f32_e32 v119, v119, v128
	v_add_f32_e32 v128, v129, v130
	v_add_f32_e32 v119, v119, v128
	v_fmamk_f32 v119, v119, 0x3b000000, v213
	v_mul_f32_e32 v128, 0x4f800000, v119
	v_cmp_gt_f32_e32 vcc, s90, v119
	s_nop 1
	v_cndmask_b32_e32 v119, v119, v128, vcc
	v_sqrt_f32_e32 v128, v119
	s_nop 0
	v_add_u32_e32 v117, -1, v128
	v_add_u32_e32 v118, 1, v128
	v_fma_f32 v129, -v117, v128, v119
	v_fma_f32 v130, -v118, v128, v119
	v_cmp_ge_f32_e64 s[14:15], 0, v129
	s_nop 1
	v_cndmask_b32_e64 v117, v128, v117, s[14:15]
	v_cmp_lt_f32_e64 s[14:15], 0, v130
	s_nop 1
	v_cndmask_b32_e64 v117, v117, v118, s[14:15]
	v_mul_f32_e32 v118, 0x37800000, v117
	v_cndmask_b32_e32 v117, v117, v118, vcc
	v_cmp_class_f32_e32 vcc, v119, v215
	s_nop 1
	v_cndmask_b32_e32 v117, v117, v119, vcc
	v_div_scale_f32 v118, s[14:15], v117, v117, 1.0
	v_rcp_f32_e32 v119, v118
	v_div_scale_f32 v113, vcc, 1.0, v117, 1.0
	v_fma_f32 v128, -v118, v119, 1.0
	v_fmac_f32_e32 v119, v128, v119
	v_mul_f32_e32 v128, v113, v119
	v_fma_f32 v129, -v118, v128, v113
	v_fmac_f32_e32 v128, v129, v119
	v_fma_f32 v113, -v118, v128, v113
	v_div_fmas_f32 v113, v113, v119, v128
	v_div_fixup_f32 v226, v113, v117, 1.0
	s_and_b64 vcc, exec, s[8:9]
	v_mul_f32_e32 v113, v226, v226
	s_cbranch_vccnz .LBB0_434
	s_and_b64 vcc, exec, s[6:7]
	v_mul_f32_e32 v117, v112, v113
	s_cbranch_vccnz .LBB0_433
	v_lshlrev_b32_e32 v131, 16, v172
	v_and_b32_e32 v135, 0xffff0000, v172
	v_and_b32_e32 v134, 0xffff0000, v174
	v_lshlrev_b32_e32 v137, 16, v173
	v_and_b32_e32 v129, 0xffff0000, v173
	v_and_b32_e32 v128, 0xffff0000, v175
	v_lshlrev_b32_e32 v130, 16, v174
	v_lshlrev_b32_e32 v136, 16, v175
	v_pk_mul_f32 v[118:119], v[134:135], v[134:135]
	v_pk_mul_f32 v[128:129], v[128:129], v[128:129]
	v_pk_fma_f32 v[118:119], v[130:131], v[130:131], v[118:119]
	v_pk_fma_f32 v[128:129], v[136:137], v[136:137], v[128:129]
	s_nop 0
	v_pk_add_f32 v[118:119], v[118:119], v[128:129]
	s_nop 0
	v_add_f32_e32 v117, v117, v118
	v_add_f32_e32 v117, v117, v119

.LBB0_440:
	s_or_b64 exec, exec, s[14:15]
	v_add_u32_e32 v112, 0x80, v232
	s_waitcnt lgkmcnt(0)
	v_ashrrev_i32_e32 v113, 31, v112
	v_lshlrev_b64 v[118:119], 6, v[112:113]
	v_lshl_add_u64 v[118:119], s[16:17], 0, v[118:119]
	global_load_dwordx4 v[128:131], v[118:119], off
	global_load_dwordx4 v[134:137], v[118:119], off offset:16
	global_load_dwordx4 v[140:143], v[118:119], off offset:1024
	global_load_dwordx4 v[144:147], v[118:119], off offset:1040
	global_load_dwordx4 v[148:151], v[118:119], off offset:2048
	global_load_dwordx4 v[192:195], v[118:119], off offset:2064
	global_load_dwordx4 v[242:245], v[118:119], off offset:3072
	global_load_dwordx4 v[246:249], v[118:119], off offset:3088
	v_mul_f32_e32 v113, v61, v61
	v_mul_f32_e32 v117, v63, v63
	v_mul_f32_e32 v118, v57, v57
	v_mul_f32_e32 v119, v59, v59
	v_fmac_f32_e32 v113, v60, v60
	v_fmac_f32_e32 v117, v62, v62
	v_fmac_f32_e32 v118, v56, v56
	v_fmac_f32_e32 v119, v58, v58
	v_add_f32_e32 v113, v113, v117
	v_add_f32_e32 v117, v118, v119
	v_add_f32_e32 v113, v113, v117
	s_mov_b64 s[26:27], -1
	s_waitcnt vmcnt(7)
	v_add_f32_e32 v128, v128, v129
	v_add_f32_e32 v129, v130, v131
	s_waitcnt vmcnt(6)
	v_add_f32_e32 v130, v134, v135
	v_add_f32_e32 v131, v136, v137
	v_add_f32_e32 v128, v128, v129
	v_add_f32_e32 v129, v130, v131
	v_add_f32_e32 v128, v128, v129
	v_fmamk_f32 v128, v128, 0x3b000000, v213
	v_mul_f32_e32 v129, 0x4f800000, v128
	v_cmp_gt_f32_e32 vcc, s90, v128
	s_nop 1
	v_cndmask_b32_e32 v128, v128, v129, vcc
	v_sqrt_f32_e32 v129, v128
	s_nop 0
	v_add_u32_e32 v118, -1, v129
	v_add_u32_e32 v119, 1, v129
	v_fma_f32 v130, -v118, v129, v128
	v_fma_f32 v131, -v119, v129, v128
	v_cmp_ge_f32_e64 s[14:15], 0, v130
	s_nop 1
	v_cndmask_b32_e64 v118, v129, v118, s[14:15]
	v_cmp_lt_f32_e64 s[14:15], 0, v131
	s_nop 1
	v_cndmask_b32_e64 v118, v118, v119, s[14:15]
	v_mul_f32_e32 v119, 0x37800000, v118
	v_cndmask_b32_e32 v118, v118, v119, vcc
	v_cmp_class_f32_e32 vcc, v128, v215
	s_nop 1
	v_cndmask_b32_e32 v118, v118, v128, vcc
	v_div_scale_f32 v119, s[14:15], v118, v118, 1.0
	v_rcp_f32_e32 v128, v119
	v_div_scale_f32 v117, vcc, 1.0, v118, 1.0
	v_fma_f32 v129, -v119, v128, 1.0
	v_fmac_f32_e32 v128, v129, v128
	v_mul_f32_e32 v129, v117, v128
	v_fma_f32 v130, -v119, v129, v117
	v_fmac_f32_e32 v129, v130, v128
	v_fma_f32 v117, -v119, v129, v117
	v_div_fmas_f32 v117, v117, v128, v129
	v_div_fixup_f32 v220, v117, v118, 1.0
	s_and_b64 vcc, exec, s[8:9]
	v_mul_f32_e32 v117, v220, v220
	s_cbranch_vccnz .LBB0_444
	s_and_b64 vcc, exec, s[6:7]
	v_mul_f32_e32 v118, v113, v117
	s_cbranch_vccnz .LBB0_443
	v_lshlrev_b32_e32 v135, 16, v176
	v_and_b32_e32 v137, 0xffff0000, v176
	v_and_b32_e32 v136, 0xffff0000, v178
	v_lshlrev_b32_e32 v139, 16, v177
	v_and_b32_e32 v131, 0xffff0000, v177
	v_and_b32_e32 v130, 0xffff0000, v179
	v_lshlrev_b32_e32 v134, 16, v178
	v_lshlrev_b32_e32 v138, 16, v179
	v_pk_mul_f32 v[128:129], v[136:137], v[136:137]
	v_pk_mul_f32 v[130:131], v[130:131], v[130:131]
	v_pk_fma_f32 v[128:129], v[134:135], v[134:135], v[128:129]
	v_pk_fma_f32 v[130:131], v[138:139], v[138:139], v[130:131]
	s_nop 0
	v_pk_add_f32 v[128:129], v[128:129], v[130:131]
	s_nop 0
	v_add_f32_e32 v112, v118, v128
	v_add_f32_e32 v118, v112, v129

.LBB0_450:
	s_or_b64 exec, exec, s[14:15]
	v_add_u32_e32 v112, 0x90, v232
	s_waitcnt lgkmcnt(0)
	v_ashrrev_i32_e32 v113, 31, v112
	v_lshlrev_b64 v[118:119], 6, v[112:113]
	v_lshl_add_u64 v[118:119], s[16:17], 0, v[118:119]
	v_mul_f32_e32 v113, v45, v45
	v_mul_f32_e32 v117, v47, v47
	v_mul_f32_e32 v118, v41, v41
	v_mul_f32_e32 v119, v43, v43
	v_fmac_f32_e32 v113, v44, v44
	v_fmac_f32_e32 v117, v46, v46
	v_fmac_f32_e32 v118, v40, v40
	v_fmac_f32_e32 v119, v42, v42
	v_add_f32_e32 v113, v113, v117
	v_add_f32_e32 v117, v118, v119
	v_add_f32_e32 v113, v113, v117
	s_mov_b64 s[26:27], -1
	s_waitcnt vmcnt(5)
	v_add_f32_e32 v128, v140, v141
	v_add_f32_e32 v129, v142, v143
	s_waitcnt vmcnt(4)
	v_add_f32_e32 v130, v144, v145
	v_add_f32_e32 v131, v146, v147
	v_add_f32_e32 v128, v128, v129
	v_add_f32_e32 v129, v130, v131
	v_add_f32_e32 v128, v128, v129
	v_fmamk_f32 v128, v128, 0x3b000000, v213
	v_mul_f32_e32 v129, 0x4f800000, v128
	v_cmp_gt_f32_e32 vcc, s90, v128
	s_nop 1
	v_cndmask_b32_e32 v128, v128, v129, vcc
	v_sqrt_f32_e32 v129, v128
	s_nop 0
	v_add_u32_e32 v118, -1, v129
	v_add_u32_e32 v119, 1, v129
	v_fma_f32 v130, -v118, v129, v128
	v_fma_f32 v131, -v119, v129, v128
	v_cmp_ge_f32_e64 s[14:15], 0, v130
	s_nop 1
	v_cndmask_b32_e64 v118, v129, v118, s[14:15]
	v_cmp_lt_f32_e64 s[14:15], 0, v131
	s_nop 1
	v_cndmask_b32_e64 v118, v118, v119, s[14:15]
	v_mul_f32_e32 v119, 0x37800000, v118
	v_cndmask_b32_e32 v118, v118, v119, vcc
	v_cmp_class_f32_e32 vcc, v128, v215
	s_nop 1
	v_cndmask_b32_e32 v118, v118, v128, vcc
	v_div_scale_f32 v119, s[14:15], v118, v118, 1.0
	v_rcp_f32_e32 v128, v119
	v_div_scale_f32 v117, vcc, 1.0, v118, 1.0
	v_fma_f32 v129, -v119, v128, 1.0
	v_fmac_f32_e32 v128, v129, v128
	v_mul_f32_e32 v129, v117, v128
	v_fma_f32 v130, -v119, v129, v117
	v_fmac_f32_e32 v129, v130, v128
	v_fma_f32 v117, -v119, v129, v117
	v_div_fmas_f32 v117, v117, v128, v129
	v_div_fixup_f32 v214, v117, v118, 1.0
	s_and_b64 vcc, exec, s[8:9]
	v_mul_f32_e32 v117, v214, v214
	s_cbranch_vccnz .LBB0_454
	s_and_b64 vcc, exec, s[6:7]
	v_mul_f32_e32 v118, v113, v117
	s_cbranch_vccnz .LBB0_453
	v_lshlrev_b32_e32 v135, 16, v180
	v_and_b32_e32 v137, 0xffff0000, v180
	v_and_b32_e32 v136, 0xffff0000, v182
	v_lshlrev_b32_e32 v139, 16, v181
	v_and_b32_e32 v131, 0xffff0000, v181
	v_and_b32_e32 v130, 0xffff0000, v183
	v_lshlrev_b32_e32 v134, 16, v182
	v_lshlrev_b32_e32 v138, 16, v183
	v_pk_mul_f32 v[128:129], v[136:137], v[136:137]
	v_pk_mul_f32 v[130:131], v[130:131], v[130:131]
	v_pk_fma_f32 v[128:129], v[134:135], v[134:135], v[128:129]
	v_pk_fma_f32 v[130:131], v[138:139], v[138:139], v[130:131]
	s_nop 0
	v_pk_add_f32 v[128:129], v[128:129], v[130:131]
	s_nop 0
	v_add_f32_e32 v112, v118, v128
	v_add_f32_e32 v118, v112, v129

.LBB0_460:
	s_or_b64 exec, exec, s[14:15]
	v_add_u32_e32 v112, 0xa0, v232
	s_waitcnt lgkmcnt(0)
	v_ashrrev_i32_e32 v113, 31, v112
	v_lshlrev_b64 v[118:119], 6, v[112:113]
	v_lshl_add_u64 v[118:119], s[16:17], 0, v[118:119]
	v_mul_f32_e32 v113, v29, v29
	v_mul_f32_e32 v117, v31, v31
	v_mul_f32_e32 v118, v25, v25
	v_mul_f32_e32 v119, v27, v27
	v_fmac_f32_e32 v113, v28, v28
	v_fmac_f32_e32 v117, v30, v30
	v_fmac_f32_e32 v118, v24, v24
	v_fmac_f32_e32 v119, v26, v26
	v_add_f32_e32 v113, v113, v117
	v_add_f32_e32 v117, v118, v119
	v_add_f32_e32 v113, v113, v117
	s_mov_b64 s[26:27], -1
	s_waitcnt vmcnt(3)
	v_add_f32_e32 v128, v148, v149
	v_add_f32_e32 v129, v150, v151
	s_waitcnt vmcnt(2)
	v_add_f32_e32 v130, v192, v193
	v_add_f32_e32 v131, v194, v195
	v_add_f32_e32 v128, v128, v129
	v_add_f32_e32 v129, v130, v131
	v_add_f32_e32 v128, v128, v129
	v_fmamk_f32 v128, v128, 0x3b000000, v213
	v_mul_f32_e32 v129, 0x4f800000, v128
	v_cmp_gt_f32_e32 vcc, s90, v128
	s_nop 1
	v_cndmask_b32_e32 v128, v128, v129, vcc
	v_sqrt_f32_e32 v129, v128
	s_nop 0
	v_add_u32_e32 v118, -1, v129
	v_add_u32_e32 v119, 1, v129
	v_fma_f32 v130, -v118, v129, v128
	v_fma_f32 v131, -v119, v129, v128
	v_cmp_ge_f32_e64 s[14:15], 0, v130
	s_nop 1
	v_cndmask_b32_e64 v118, v129, v118, s[14:15]
	v_cmp_lt_f32_e64 s[14:15], 0, v131
	s_nop 1
	v_cndmask_b32_e64 v118, v118, v119, s[14:15]
	v_mul_f32_e32 v119, 0x37800000, v118
	v_cndmask_b32_e32 v118, v118, v119, vcc
	v_cmp_class_f32_e32 vcc, v128, v215
	s_nop 1
	v_cndmask_b32_e32 v118, v118, v128, vcc
	v_div_scale_f32 v119, s[14:15], v118, v118, 1.0
	v_rcp_f32_e32 v128, v119
	v_div_scale_f32 v117, vcc, 1.0, v118, 1.0
	v_fma_f32 v129, -v119, v128, 1.0
	v_fmac_f32_e32 v128, v129, v128
	v_mul_f32_e32 v129, v117, v128
	v_fma_f32 v130, -v119, v129, v117
	v_fmac_f32_e32 v129, v130, v128
	v_fma_f32 v117, -v119, v129, v117
	v_div_fmas_f32 v117, v117, v128, v129
	v_div_fixup_f32 v212, v117, v118, 1.0
	s_and_b64 vcc, exec, s[8:9]
	v_mul_f32_e32 v117, v212, v212
	s_cbranch_vccnz .LBB0_464
	s_and_b64 vcc, exec, s[6:7]
	v_mul_f32_e32 v118, v113, v117
	s_cbranch_vccnz .LBB0_463
	v_lshlrev_b32_e32 v135, 16, v184
	v_and_b32_e32 v137, 0xffff0000, v184
	v_and_b32_e32 v136, 0xffff0000, v186
	v_lshlrev_b32_e32 v139, 16, v185
	v_and_b32_e32 v131, 0xffff0000, v185
	v_and_b32_e32 v130, 0xffff0000, v187
	v_lshlrev_b32_e32 v134, 16, v186
	v_lshlrev_b32_e32 v138, 16, v187
	v_pk_mul_f32 v[128:129], v[136:137], v[136:137]
	v_pk_mul_f32 v[130:131], v[130:131], v[130:131]
	v_pk_fma_f32 v[128:129], v[134:135], v[134:135], v[128:129]
	v_pk_fma_f32 v[130:131], v[138:139], v[138:139], v[130:131]
	s_nop 0
	v_pk_add_f32 v[128:129], v[128:129], v[130:131]
	s_nop 0
	v_add_f32_e32 v112, v118, v128
	v_add_f32_e32 v118, v112, v129

.LBB0_470:
	s_or_b64 exec, exec, s[14:15]
	v_add_u32_e32 v112, 0xb0, v232
	s_waitcnt lgkmcnt(0)
	v_ashrrev_i32_e32 v113, 31, v112
	v_lshlrev_b64 v[116:117], 6, v[112:113]
	v_lshl_add_u64 v[128:129], s[16:17], 0, v[116:117]
	s_nop 0
	v_mul_f32_e32 v113, v13, v13
	v_mul_f32_e32 v133, v15, v15
	v_mul_f32_e32 v134, v9, v9
	v_mul_f32_e32 v135, v11, v11
	v_fmac_f32_e32 v113, v12, v12
	v_fmac_f32_e32 v133, v14, v14
	v_fmac_f32_e32 v134, v8, v8
	v_fmac_f32_e32 v135, v10, v10
	v_add_f32_e32 v113, v113, v133
	s_mov_b64 s[14:15], -1
	s_waitcnt vmcnt(1)
	v_add_f32_e32 v116, v242, v243
	v_add_f32_e32 v117, v244, v245
	s_waitcnt vmcnt(0)
	v_add_f32_e32 v118, v246, v247
	v_add_f32_e32 v119, v248, v249
	v_add_f32_e32 v116, v116, v117
	v_add_f32_e32 v117, v118, v119
	v_add_f32_e32 v116, v116, v117
	v_fmamk_f32 v116, v116, 0x3b000000, v213
	v_mul_f32_e32 v117, 0x4f800000, v116
	v_cmp_gt_f32_e32 vcc, s90, v116
	v_add_f32_e32 v118, v134, v135
	v_add_f32_e32 v113, v113, v118
	v_cndmask_b32_e32 v116, v116, v117, vcc
	v_sqrt_f32_e32 v117, v116
	s_nop 0
	v_add_u32_e32 v119, -1, v117
	v_add_u32_e32 v128, 1, v117
	v_fma_f32 v129, -v119, v117, v116
	v_fma_f32 v130, -v128, v117, v116
	v_cmp_ge_f32_e64 s[12:13], 0, v129
	s_nop 1
	v_cndmask_b32_e64 v117, v117, v119, s[12:13]
	v_cmp_lt_f32_e64 s[12:13], 0, v130
	s_nop 1
	v_cndmask_b32_e64 v117, v117, v128, s[12:13]
	v_mul_f32_e32 v119, 0x37800000, v117
	v_cndmask_b32_e32 v117, v117, v119, vcc
	v_cmp_class_f32_e32 vcc, v116, v215
	s_nop 1
	v_cndmask_b32_e32 v116, v117, v116, vcc
	v_div_scale_f32 v117, s[12:13], v116, v116, 1.0
	v_rcp_f32_e32 v119, v117
	v_div_scale_f32 v118, vcc, 1.0, v116, 1.0
	v_fma_f32 v128, -v117, v119, 1.0
	v_fmac_f32_e32 v119, v128, v119
	v_mul_f32_e32 v128, v118, v119
	v_fma_f32 v129, -v117, v128, v118
	v_fmac_f32_e32 v128, v129, v119
	v_fma_f32 v117, -v117, v128, v118
	v_div_fmas_f32 v117, v117, v119, v128
	v_div_fixup_f32 v210, v117, v116, 1.0
	s_and_b64 vcc, exec, s[8:9]
	v_mul_f32_e32 v116, v210, v210
	s_cbranch_vccnz .LBB0_474
	s_and_b64 vcc, exec, s[6:7]
	v_mul_f32_e32 v117, v113, v116
	s_cbranch_vccnz .LBB0_473
	v_lshlrev_b32_e32 v131, 16, v188
	v_and_b32_e32 v135, 0xffff0000, v188
	v_and_b32_e32 v134, 0xffff0000, v190
	v_lshlrev_b32_e32 v137, 16, v189
	v_and_b32_e32 v129, 0xffff0000, v189
	v_and_b32_e32 v128, 0xffff0000, v191
	v_lshlrev_b32_e32 v130, 16, v190
	v_lshlrev_b32_e32 v136, 16, v191
	v_pk_mul_f32 v[118:119], v[134:135], v[134:135]
	v_pk_mul_f32 v[128:129], v[128:129], v[128:129]
	v_pk_fma_f32 v[118:119], v[130:131], v[130:131], v[118:119]
	v_pk_fma_f32 v[128:129], v[136:137], v[136:137], v[128:129]
	s_nop 0
	v_pk_add_f32 v[118:119], v[118:119], v[128:129]
	s_nop 0
	v_add_f32_e32 v112, v117, v118
	v_add_f32_e32 v117, v112, v119
